# same as v11 with exp weighted 16 cycles in filler distribution
# speedup vs baseline: 1.0036x; 1.0036x over previous
.Lat_back0_s0:
	v_sub_f32_e32 v144, v144, v209
	v_sub_f32_e32 v145, v145, v209
	v_sub_f32_e32 v146, v146, v209
	v_sub_f32_e32 v147, v147, v209
	v_exp_f32_e32 v144, v144
	v_exp_f32_e32 v145, v145
	v_exp_f32_e32 v146, v146
	v_exp_f32_e32 v147, v147
	v_sub_f32_e32 v148, v148, v209
	v_sub_f32_e32 v149, v149, v209
	v_sub_f32_e32 v150, v150, v209
	v_sub_f32_e32 v151, v151, v209
	v_exp_f32_e32 v148, v148
	v_exp_f32_e32 v149, v149
	v_exp_f32_e32 v150, v150
	v_exp_f32_e32 v151, v151
	s_waitcnt lgkmcnt(0)
	v_mfma_f32_32x32x16_bf16 v[160:175], v[228:231], v[244:247], 0
	v_sub_f32_e32 v152, v152, v209
	v_sub_f32_e32 v153, v153, v209
	v_sub_f32_e32 v154, v154, v209
	v_sub_f32_e32 v155, v155, v209
	v_exp_f32_e32 v152, v152
	v_exp_f32_e32 v153, v153
	v_exp_f32_e32 v154, v154
	v_mfma_f32_32x32x16_bf16 v[160:175], v[232:235], v[248:251], v[160:175]
	v_exp_f32_e32 v155, v155
	v_sub_f32_e32 v156, v156, v209
	v_sub_f32_e32 v157, v157, v209
	v_sub_f32_e32 v158, v158, v209
	v_sub_f32_e32 v159, v159, v209
	v_exp_f32_e32 v156, v156
	v_exp_f32_e32 v157, v157
	v_mfma_f32_32x32x16_bf16 v[160:175], v[236:239], v[4:7], v[160:175]
	v_exp_f32_e32 v158, v158
	v_exp_f32_e32 v159, v159
	v_add_f32_e32 v15, v144, v145
	v_add_f32_e32 v211, v146, v147
	v_add_f32_e32 v15, v15, v211
	v_add_f32_e32 v211, v148, v149
	v_add_f32_e32 v224, v150, v151
	v_add_f32_e32 v211, v211, v224
	v_add_f32_e32 v224, v152, v153
	v_add_f32_e32 v225, v154, v155
	v_mfma_f32_32x32x16_bf16 v[160:175], v[240:243], v[8:11], v[160:175]
	v_add_f32_e32 v224, v224, v225
	v_add_f32_e32 v225, v156, v157
	v_add_f32_e32 v227, v158, v159
	v_add_f32_e32 v225, v225, v227
	v_add_f32_e32 v15, v15, v211
	v_add_f32_e32 v224, v224, v225
	v_add_f32_e32 v15, v15, v224
	v_add_f32_e32 v210, v210, v15
	v_cvt_pk_bf16_f32 v144, v144, v145
	v_cvt_pk_bf16_f32 v145, v146, v147
	v_cvt_pk_bf16_f32 v146, v148, v149
	v_cvt_pk_bf16_f32 v147, v150, v151
	v_cvt_pk_bf16_f32 v148, v152, v153
	v_cvt_pk_bf16_f32 v149, v154, v155
	v_cvt_pk_bf16_f32 v150, v156, v157
	v_cvt_pk_bf16_f32 v151, v158, v159
	s_nop 1
	v_mfma_f32_32x32x16_bf16 v[128:143], v[184:187], v[144:147], v[128:143]
	ds_read_b128 v[228:231], v12 offset:8704
	ds_read_b128 v[232:235], v12 offset:8736
	ds_read_b128 v[236:239], v12 offset:8768
	ds_read_b128 v[240:243], v12 offset:8800
	ds_read_b128 v[244:247], v13 offset:0
	ds_read_b128 v[248:251], v13 offset:32
	ds_read_b128 v[4:7], v13 offset:64
	ds_read_b128 v[8:11], v13 offset:96
	v_max3_f32 v15, v160, v161, v162
	v_max3_f32 v211, v163, v164, v165
	v_max3_f32 v224, v166, v167, v168
	v_max3_f32 v225, v169, v170, v171
	v_mfma_f32_32x32x16_bf16 v[96:111], v[188:191], v[144:147], v[96:111]
	v_max3_f32 v227, v172, v173, v174
	v_max3_f32 v15, v15, v211, v175
	v_max3_f32 v224, v224, v225, v227
	v_max_f32_e32 v15, v15, v224
	v_mov_b32_e32 v211, v15
	v_add_f32_e32 v225, 0x41000000, v208
	s_nop 1
	v_permlane32_swap_b32_e32 v15, v211
	v_max_f32_e32 v15, v15, v211
	v_cmp_gt_f32_e32 vcc, v15, v225
	s_cbranch_vccnz .Lat_slow1_s0
.Lat_back1_s0:
	v_sub_f32_e32 v160, v160, v208
	v_mfma_f32_32x32x16_bf16 v[64:79], v[192:195], v[144:147], v[64:79]
	v_sub_f32_e32 v161, v161, v208
	v_sub_f32_e32 v162, v162, v208
	v_sub_f32_e32 v163, v163, v208
	v_exp_f32_e32 v160, v160
	v_exp_f32_e32 v161, v161
	v_exp_f32_e32 v162, v162
	v_mfma_f32_32x32x16_bf16 v[32:47], v[196:199], v[144:147], v[32:47]
	v_exp_f32_e32 v163, v163
	v_sub_f32_e32 v164, v164, v208
	v_sub_f32_e32 v165, v165, v208
	v_sub_f32_e32 v166, v166, v208
	v_sub_f32_e32 v167, v167, v208
	v_exp_f32_e32 v164, v164
	v_mfma_f32_32x32x16_bf16 v[128:143], v[200:203], v[148:151], v[128:143]
	v_exp_f32_e32 v165, v165
	v_exp_f32_e32 v166, v166
	v_exp_f32_e32 v167, v167
	v_mfma_f32_32x32x16_bf16 v[96:111], v[212:215], v[148:151], v[96:111]
	v_sub_f32_e32 v168, v168, v208
	v_sub_f32_e32 v169, v169, v208
	v_sub_f32_e32 v170, v170, v208
	v_sub_f32_e32 v171, v171, v208
	v_exp_f32_e32 v168, v168
	v_exp_f32_e32 v169, v169
	v_mfma_f32_32x32x16_bf16 v[64:79], v[216:219], v[148:151], v[64:79]
	v_exp_f32_e32 v170, v170
	v_exp_f32_e32 v171, v171
	v_sub_f32_e32 v172, v172, v208
	v_mfma_f32_32x32x16_bf16 v[32:47], v[220:223], v[148:151], v[32:47]
	v_sub_f32_e32 v173, v173, v208
	v_sub_f32_e32 v174, v174, v208
	v_sub_f32_e32 v175, v175, v208
	v_exp_f32_e32 v172, v172
	v_exp_f32_e32 v173, v173
	s_waitcnt lgkmcnt(0)
	v_mfma_f32_32x32x16_bf16 v[144:159], v[228:231], v[244:247], 0
	v_exp_f32_e32 v174, v174
	v_exp_f32_e32 v175, v175
	v_add_f32_e32 v15, v160, v161
	v_add_f32_e32 v211, v162, v163
	v_add_f32_e32 v15, v15, v211
	v_mfma_f32_32x32x16_bf16 v[144:159], v[232:235], v[248:251], v[144:159]
	v_add_f32_e32 v211, v164, v165
	v_add_f32_e32 v224, v166, v167
	v_add_f32_e32 v211, v211, v224
	v_add_f32_e32 v224, v168, v169
	v_add_f32_e32 v225, v170, v171
	v_add_f32_e32 v224, v224, v225
	v_add_f32_e32 v225, v172, v173
	v_add_f32_e32 v227, v174, v175
	v_add_f32_e32 v225, v225, v227
	v_add_f32_e32 v15, v15, v211
	v_add_f32_e32 v224, v224, v225
	v_mfma_f32_32x32x16_bf16 v[144:159], v[236:239], v[4:7], v[144:159]
	v_add_f32_e32 v15, v15, v224
	v_add_f32_e32 v207, v207, v15
	v_cvt_pk_bf16_f32 v160, v160, v161
	v_cvt_pk_bf16_f32 v161, v162, v163
	v_cvt_pk_bf16_f32 v162, v164, v165
	v_cvt_pk_bf16_f32 v163, v166, v167
	v_cvt_pk_bf16_f32 v164, v168, v169
	v_cvt_pk_bf16_f32 v165, v170, v171
	v_cvt_pk_bf16_f32 v166, v172, v173
	v_cvt_pk_bf16_f32 v167, v174, v175
	v_mfma_f32_32x32x16_bf16 v[144:159], v[240:243], v[8:11], v[144:159]
	s_nop 1
	v_mfma_f32_32x32x16_bf16 v[112:127], v[184:187], v[160:163], v[112:127]
	ds_read_b128 v[228:231], v12 offset:8832
	ds_read_b128 v[232:235], v12 offset:8864
	ds_read_b128 v[236:239], v12 offset:8896
	ds_read_b128 v[240:243], v12 offset:8928
	ds_read_b128 v[244:247], v13 offset:128
	ds_read_b128 v[248:251], v13 offset:160
	ds_read_b128 v[4:7], v13 offset:192
	ds_read_b128 v[8:11], v13 offset:224
	s_nop 3
	v_max3_f32 v15, v144, v145, v146
	v_max3_f32 v211, v147, v148, v149
	v_max3_f32 v224, v150, v151, v152
	v_mfma_f32_32x32x16_bf16 v[80:95], v[188:191], v[160:163], v[80:95]
	v_max3_f32 v225, v153, v154, v155
	v_max3_f32 v227, v156, v157, v158
	v_max3_f32 v15, v15, v211, v159
	v_max3_f32 v224, v224, v225, v227
	v_max_f32_e32 v15, v15, v224
	v_mov_b32_e32 v211, v15
	v_add_f32_e32 v225, 0x41000000, v209
	s_nop 1
	v_permlane32_swap_b32_e32 v15, v211
	v_max_f32_e32 v15, v15, v211
	v_cmp_gt_f32_e32 vcc, v15, v225
	s_cbranch_vccnz .Lat_slow0_s1
.Lat_back0_s1:
	v_mfma_f32_32x32x16_bf16 v[48:63], v[192:195], v[160:163], v[48:63]
	v_sub_f32_e32 v144, v144, v209
	v_sub_f32_e32 v145, v145, v209
	v_sub_f32_e32 v146, v146, v209
	v_sub_f32_e32 v147, v147, v209
	v_exp_f32_e32 v144, v144
	v_exp_f32_e32 v145, v145
	v_mfma_f32_32x32x16_bf16 v[16:31], v[196:199], v[160:163], v[16:31]
	v_exp_f32_e32 v146, v146
	v_exp_f32_e32 v147, v147
	v_sub_f32_e32 v148, v148, v209
	v_sub_f32_e32 v149, v149, v209
	v_sub_f32_e32 v150, v150, v209
	v_sub_f32_e32 v151, v151, v209
	v_mfma_f32_32x32x16_bf16 v[112:127], v[200:203], v[164:167], v[112:127]
	v_exp_f32_e32 v148, v148
	v_exp_f32_e32 v149, v149
	v_exp_f32_e32 v150, v150
	v_mfma_f32_32x32x16_bf16 v[80:95], v[212:215], v[164:167], v[80:95]
	v_exp_f32_e32 v151, v151
	v_sub_f32_e32 v152, v152, v209
	v_sub_f32_e32 v153, v153, v209
	v_sub_f32_e32 v154, v154, v209
	v_sub_f32_e32 v155, v155, v209
	v_exp_f32_e32 v152, v152
	v_mfma_f32_32x32x16_bf16 v[48:63], v[216:219], v[164:167], v[48:63]
	v_exp_f32_e32 v153, v153
	v_exp_f32_e32 v154, v154
	v_exp_f32_e32 v155, v155
	v_mfma_f32_32x32x16_bf16 v[16:31], v[220:223], v[164:167], v[16:31]
	v_sub_f32_e32 v156, v156, v209
	v_sub_f32_e32 v157, v157, v209
	v_sub_f32_e32 v158, v158, v209
	v_sub_f32_e32 v159, v159, v209
	v_exp_f32_e32 v156, v156
	v_exp_f32_e32 v157, v157
	ds_read_b128 v[184:187], v14 offset:34880
	ds_read_b128 v[188:191], v14 offset:39488
	ds_read_b128 v[192:195], v14 offset:44096
	ds_read_b128 v[196:199], v14 offset:48704
	ds_read_b128 v[200:203], v14 offset:34912
	ds_read_b128 v[212:215], v14 offset:39520
	ds_read_b128 v[216:219], v14 offset:44128
	s_waitcnt lgkmcnt(7)
	ds_read_b128 v[220:223], v14 offset:48736
	v_mfma_f32_32x32x16_bf16 v[160:175], v[228:231], v[244:247], 0
	v_exp_f32_e32 v158, v158
	v_exp_f32_e32 v159, v159
	v_add_f32_e32 v15, v144, v145
	v_add_f32_e32 v211, v146, v147
	v_add_f32_e32 v15, v15, v211
	v_mfma_f32_32x32x16_bf16 v[160:175], v[232:235], v[248:251], v[160:175]
	v_add_f32_e32 v211, v148, v149
	v_add_f32_e32 v224, v150, v151
	v_add_f32_e32 v211, v211, v224
	v_add_f32_e32 v224, v152, v153
	v_add_f32_e32 v225, v154, v155
	v_add_f32_e32 v224, v224, v225
	v_add_f32_e32 v225, v156, v157
	v_add_f32_e32 v227, v158, v159
	v_add_f32_e32 v225, v225, v227
	v_add_f32_e32 v15, v15, v211
	v_add_f32_e32 v224, v224, v225
	v_mfma_f32_32x32x16_bf16 v[160:175], v[236:239], v[4:7], v[160:175]
	v_add_f32_e32 v15, v15, v224
	v_add_f32_e32 v210, v210, v15
	v_cvt_pk_bf16_f32 v144, v144, v145
	v_cvt_pk_bf16_f32 v145, v146, v147
	v_cvt_pk_bf16_f32 v146, v148, v149
	v_cvt_pk_bf16_f32 v147, v150, v151
	v_cvt_pk_bf16_f32 v148, v152, v153
	v_cvt_pk_bf16_f32 v149, v154, v155
	v_cvt_pk_bf16_f32 v150, v156, v157
	v_cvt_pk_bf16_f32 v151, v158, v159
	v_mfma_f32_32x32x16_bf16 v[160:175], v[240:243], v[8:11], v[160:175]
	s_waitcnt lgkmcnt(0)
	s_nop 0
	v_mfma_f32_32x32x16_bf16 v[128:143], v[184:187], v[144:147], v[128:143]
	v_bfe_u32 v1, v204, 2, 2
	v_and_b32_e32 v2, 12, v204
	v_cmp_ne_u32_e32 vcc, 2, v1
	s_xor_b32 s8, s27, 1
	s_mulk_i32 s8, 0x4800
	v_cndmask_b32_e32 v2, 4, v2, vcc
	v_cmp_ne_u32_e32 vcc, 1, v1
	v_add_u32_e32 v15, s8, v205
	s_movk_i32 s8, 0x480
	v_cndmask_b32_e32 v1, 8, v2, vcc
	v_ashrrev_i32_e32 v2, 6, v204
	v_and_or_b32 v252, v204, 51, v1
	v_mul_lo_u32 v2, v2, s8
	v_lshlrev_b32_e32 v252, 1, v252
	v_add3_u32 v252, v15, v2, v252
	v_max3_f32 v15, v160, v161, v162
	v_max3_f32 v211, v163, v164, v165
	v_max3_f32 v224, v166, v167, v168
	v_max3_f32 v225, v169, v170, v171
	v_max3_f32 v227, v172, v173, v174
	v_mfma_f32_32x32x16_bf16 v[96:111], v[188:191], v[144:147], v[96:111]
	v_max3_f32 v15, v15, v211, v175
	v_max3_f32 v224, v224, v225, v227
	v_max_f32_e32 v15, v15, v224
	v_mov_b32_e32 v211, v15
	v_add_f32_e32 v225, 0x41000000, v208
	s_nop 1
	v_permlane32_swap_b32_e32 v15, v211
	v_max_f32_e32 v15, v15, v211
	v_cmp_gt_f32_e32 vcc, v15, v225
	s_cbranch_vccnz .Lat_slow1_s1
.Lat_back1_s1:
	v_sub_f32_e32 v160, v160, v208
	v_sub_f32_e32 v161, v161, v208
	v_sub_f32_e32 v162, v162, v208
	v_sub_f32_e32 v163, v163, v208
	v_exp_f32_e32 v160, v160
	v_exp_f32_e32 v161, v161
	v_mfma_f32_32x32x16_bf16 v[64:79], v[192:195], v[144:147], v[64:79]
	v_exp_f32_e32 v162, v162
	v_exp_f32_e32 v163, v163
	v_sub_f32_e32 v164, v164, v208
	v_sub_f32_e32 v165, v165, v208
	v_sub_f32_e32 v166, v166, v208
	v_sub_f32_e32 v167, v167, v208
	v_exp_f32_e32 v164, v164
	v_mfma_f32_32x32x16_bf16 v[32:47], v[196:199], v[144:147], v[32:47]
	v_exp_f32_e32 v165, v165
	v_exp_f32_e32 v166, v166
	v_exp_f32_e32 v167, v167
	v_sub_f32_e32 v168, v168, v208
	v_sub_f32_e32 v169, v169, v208
	v_sub_f32_e32 v170, v170, v208
	v_sub_f32_e32 v171, v171, v208
	v_exp_f32_e32 v168, v168
	v_mfma_f32_32x32x16_bf16 v[128:143], v[200:203], v[148:151], v[128:143]
	v_exp_f32_e32 v169, v169
	v_exp_f32_e32 v170, v170
	v_exp_f32_e32 v171, v171
	v_sub_f32_e32 v172, v172, v208
	v_sub_f32_e32 v173, v173, v208
	v_sub_f32_e32 v174, v174, v208
	v_sub_f32_e32 v175, v175, v208
	v_exp_f32_e32 v172, v172
	v_mfma_f32_32x32x16_bf16 v[96:111], v[212:215], v[148:151], v[96:111]
	v_exp_f32_e32 v173, v173
	v_exp_f32_e32 v174, v174
	v_exp_f32_e32 v175, v175
	v_add_f32_e32 v15, v160, v161
	v_add_f32_e32 v211, v162, v163
	v_add_f32_e32 v15, v15, v211
	v_add_f32_e32 v211, v164, v165
	v_add_f32_e32 v224, v166, v167
	v_mfma_f32_32x32x16_bf16 v[64:79], v[216:219], v[148:151], v[64:79]
	v_add_f32_e32 v211, v211, v224
	v_add_f32_e32 v224, v168, v169
	v_add_f32_e32 v225, v170, v171
	v_add_f32_e32 v224, v224, v225
	v_add_f32_e32 v225, v172, v173
	v_add_f32_e32 v227, v174, v175
	v_add_f32_e32 v225, v225, v227
	v_add_f32_e32 v15, v15, v211
	v_add_f32_e32 v224, v224, v225
	v_add_f32_e32 v15, v15, v224
	v_add_f32_e32 v207, v207, v15
	v_cvt_pk_bf16_f32 v160, v160, v161
	v_cvt_pk_bf16_f32 v161, v162, v163
	v_cvt_pk_bf16_f32 v162, v164, v165
	v_cvt_pk_bf16_f32 v163, v166, v167
	v_cvt_pk_bf16_f32 v164, v168, v169
	v_cvt_pk_bf16_f32 v165, v170, v171
	v_cvt_pk_bf16_f32 v166, v172, v173
	v_cvt_pk_bf16_f32 v167, v174, v175
	v_mfma_f32_32x32x16_bf16 v[32:47], v[220:223], v[148:151], v[32:47]
	s_nop 1
	v_mfma_f32_32x32x16_bf16 v[112:127], v[184:187], v[160:163], v[112:127]
	s_waitcnt vmcnt(0)
	ds_write_b16 v252, v176 offset:34816
	ds_write_b16_d16_hi v252, v176 offset:34960
	v_mfma_f32_32x32x16_bf16 v[80:95], v[188:191], v[160:163], v[80:95]
	ds_write_b16 v252, v177 offset:35104
	ds_write_b16_d16_hi v252, v177 offset:35248
	v_mfma_f32_32x32x16_bf16 v[48:63], v[192:195], v[160:163], v[48:63]
	ds_write_b16 v252, v178 offset:35392
	ds_write_b16_d16_hi v252, v178 offset:35536
	v_mfma_f32_32x32x16_bf16 v[16:31], v[196:199], v[160:163], v[16:31]
	ds_write_b16 v252, v179 offset:35680
	ds_write_b16_d16_hi v252, v179 offset:35824
	v_mfma_f32_32x32x16_bf16 v[112:127], v[200:203], v[164:167], v[112:127]
	ds_write_b16 v252, v180 offset:44032
	ds_write_b16_d16_hi v252, v180 offset:44176
	v_mfma_f32_32x32x16_bf16 v[80:95], v[212:215], v[164:167], v[80:95]
	ds_write_b16 v252, v181 offset:44320
	ds_write_b16_d16_hi v252, v181 offset:44464
	v_mfma_f32_32x32x16_bf16 v[48:63], v[216:219], v[164:167], v[48:63]
	ds_write_b16 v252, v182 offset:44608
	ds_write_b16_d16_hi v252, v182 offset:44752
	v_mfma_f32_32x32x16_bf16 v[16:31], v[220:223], v[164:167], v[16:31]
	ds_write_b16 v252, v183 offset:44896
	ds_write_b16_d16_hi v252, v183 offset:45040
	s_add_i32 s23, s23, 64
	s_cmpk_lg_i32 s23, 0x1100
	s_waitcnt vmcnt(0) lgkmcnt(0)
	s_barrier
	s_cbranch_scc0 .Lat_exit
	s_mov_b32 s26, s25
	s_branch .LBB0_439
